# proj phase with 48 helpers / 208 workers (15 rounds) converting 23296 items; down phase back to 64 helpers / 6 rounds
# speedup vs baseline: 1.0091x; 1.0091x over previous
;     ...
;         const int gw = vcu * NWAVES + wave, NGW = G * NWAVES;
;         constexpr int C_IN = 32 * 188, C_OA = 8 * 32, C_OB = 16 * 32, C_O = 32 * 32, C_GU = 16 * 32 * 32, C_DN = 16 * 16 * 32, C_L = C_IN + C_OA + C_OB + C_O + C_GU + C_DN, NIT = DEPTH * C_L;
;         const int q4 = lane & 15, kk = lane >> 4;
;         auto decode = [&](int it) -> TrDesc {
;             TrDesc d; d.zero = 0; d.rope = 0; d.f8 = 0;
;             const int l = it / C_L; int r = it % C_L;
;             const float* W; unsigned char* WT; int ldw, K, k0, n0, scol, esz = 2;
;             if (r < C_IN) { const int kb = r / 188, nb = r % 188; n0 = 64 * nb; k0 = 64 * kb; ldw = NIN; K = D; W = a.w_in + (size_t)l * D * NIN;
;                 if (n0 < 3072) { d.rope = 1; scol = (n0 >> 7) * 128 + 32 * ((n0 >> 6) & 1) + 64 * (q4 >> 3) + 4 * (q4 & 7); }
;                 else if (n0 < 7680) scol = n0 + 4 * q4;
;                 else if (n0 < 11776) scol = n0 + 16 + 4 * q4;
;                 else if (n0 == 11776) { scol = (q4 < 4) ? 7680 + 4 * q4 : 0; d.zero = (q4 < 4) ? 0 : 1; }
;                 else { scol = 0; d.zero = 1; }
;     ...
;                 d.f8 = 1; esz = 1; WT = ws + WS_WIN + (size_t)l * NP * D;
;     ...
;                 WT = ws + WS_WIN + (size_t)l * NP * D * 2;
;     ...
;             } else if ((r -= C_IN) < C_OA) { const int kb = r / 32, nb = r % 32; n0 = 64 * nb; k0 = 64 * kb; ldw = D; K = 512; scol = n0 + 4 * q4; W = a.w_out_a + (size_t)l * 512 * D; WT = ws + WS_WOA + (size_t)l * D * 512 * (MIX_F8 ? 1 : 2); if (MIX_F8) { d.f8 = 1; esz = 1; }
;                 if (BR_FUSE) { K = 1536; WT = ws + WS_WOA + (size_t)l * D * 1536 + 1024; }
;             } else if ((r -= C_OA) < C_OB) { const int kb = r / 32, nb = r % 32; n0 = 64 * nb; k0 = 64 * kb; ldw = D; K = 1024; scol = n0 + 4 * q4; W = a.w_out_b + (size_t)l * 1024 * D; WT = ws + WS_WOB + (size_t)l * D * 1024 * (MIX_F8 ? 1 : 2); if (MIX_F8) { d.f8 = 1; esz = 1; }
; template <unsigned MASK, bool ONE>
; __global__ void __launch_bounds__(NTHREADS, 2) fwd_kernel(Args a_unused) {
;     ...
;         if (IN(P + 1, 2)) { FRESH_TID();
;     ...
;             pg8::StaticOrderP S{T / 256, NP / 256, G, bx}; pg8::RowsContig AM; pg8::EpiProj E{proj, ropec, ropes, alow, pg8::W8_INV};
;             pg8::gemm_phase<pg8::EpiProj, pg8::StaticOrderP, pg8::RowsContig, true, true>(lds, tid, hbuf, (const bf16_t*)(ws + WS_WIN + (size_t)l * NP * D), 0, D / 2, S, AM, E);
.LBB0_265:
	s_or_b64 exec, exec, s[0:1]
	v_readlane_b32 s0, v253, 0
	v_readlane_b32 s1, v253, 1
	s_mov_b32 s2, s38
	s_waitcnt lgkmcnt(0)
	s_barrier
	s_nop 0
	v_mbcnt_lo_u32_b32 v0, s2, 0
	v_mbcnt_hi_u32_b32 v0, s2, v0
	v_readlane_b32 s2, v253, 7
	v_readlane_b32 s3, v253, 8
	v_add_u32_e32 v1, s78, v0
	s_andn2_b64 vcc, exec, s[2:3]
	v_readfirstlane_b32 s16, v1
	v_readlane_b32 s101, v255, 17
	s_movk_i32 s100, 0x100
	s_cmp_eq_u32 s101, 0
	s_cbranch_scc0 .Lpq_skip
	s_movk_i32 s100, 0xd0
	v_readlane_b32 s101, v253, 4
	s_nop 1
	s_cmp_lt_i32 s101, s100
	s_cbranch_scc1 .Lpq_skip
	s_mov_b32 s100, 0x8a80
	s_mov_b32 s101, 0xe580
	v_writelane_b32 v251, s16, 0
	v_writelane_b32 v251, s17, 1
	v_writelane_b32 v251, s18, 2
	v_writelane_b32 v251, s19, 3
	v_writelane_b32 v251, s20, 4
	v_writelane_b32 v251, s21, 5
	v_writelane_b32 v251, s23, 6
	v_writelane_b32 v251, s25, 7
	v_writelane_b32 v251, s26, 8
	v_writelane_b32 v251, s33, 9
	v_writelane_b32 v251, s38, 10
	v_writelane_b32 v251, s39, 11
	v_writelane_b32 v251, s41, 12
	v_writelane_b32 v251, s42, 13
	v_writelane_b32 v251, s45, 14
	v_writelane_b32 v251, s48, 15
	v_writelane_b32 v251, s49, 16
	v_writelane_b32 v251, s50, 17
	v_writelane_b32 v251, s51, 18
	v_writelane_b32 v251, s74, 19
	v_writelane_b32 v251, s76, 20
	v_mov_b32_e32 v193, v3
	v_mov_b32_e32 v194, v33
	v_mov_b32_e32 v195, v59
	v_mov_b32_e32 v196, v63
	v_mov_b32_e32 v197, v110
	v_mov_b32_e32 v198, v111
	v_mov_b32_e32 v199, v114
	v_mov_b32_e32 v200, v115
	v_mov_b32_e32 v201, v149
	v_mov_b32_e32 v202, v153
	v_mov_b32_e32 v203, v157
	v_mov_b32_e32 v204, v161
	v_mov_b32_e32 v205, v165
	v_mov_b32_e32 v206, v169
	v_mov_b32_e32 v207, v173
	v_mov_b32_e32 v208, v177
	v_mov_b32_e32 v209, v178
	v_mov_b32_e32 v210, v179
	v_mov_b32_e32 v211, v180
	v_mov_b32_e32 v212, v181
	v_mov_b32_e32 v214, v182
	v_mov_b32_e32 v215, v183
	v_mov_b32_e32 v216, v184
	v_mov_b32_e32 v218, v185
	v_readlane_b32 s76, v253, 4
	v_readlane_b32 s8, v253, 0
	v_readlane_b32 s9, v253, 1
	s_nop 1
	s_sub_i32 s0, s76, 208
	s_lshr_b32 s1, s100, 3
	s_add_i32 s0, s0, s1
	s_lshr_b32 s33, s78, 6
	s_lshr_b32 s1, s0, 3
	s_lshl_b32 s1, s1, 6
	s_and_b32 s0, s0, 7
	s_lshl_b32 s0, s0, 2
	s_or_b32 s1, s1, s0
	s_and_b32 s0, s33, 3
	s_or_b32 s1, s1, s0
	s_lshr_b32 s0, s33, 2
	s_lshl_b32 s0, s0, 5
	s_or_b32 s1, s1, s0
	s_sub_i32 s100, s1, s33
	s_mov_b32 s76, 0
	s_movk_i32 s74, 48
	s_load_dwordx2 s[10:11], s[8:9], 0xa0
	v_mbcnt_lo_u32_b32 v69, -1, 0
	v_mbcnt_hi_u32_b32 v69, -1, v69
	s_mov_b64 exec, -1
	v_lshlrev_b32_e32 v76, 3, v69
	s_waitcnt lgkmcnt(0)
	s_lshl_b32 s47, s76, 3
	s_add_i32 s47, s47, s33
	s_add_i32 s47, s47, s100
	v_and_b32_e32 v2, 15, v69
	s_cmp_ge_i32 s47, s101
	v_ashrrev_i32_e32 v133, 4, v69
	s_cbranch_scc1 .LBB0_36_hq
	s_sub_i32 s1, 0xfcff, s47
	s_mul_hi_u32 s0, s1, 0x81848da9
	s_lshr_b32 s0, s0, 14
	s_mul_i32 s2, s0, 0x7e80
	s_sub_i32 s17, s1, s2
	s_cmpk_gt_u32 s17, 0x177f
	s_cbranch_scc0 .LBB0_37_hq
	s_cmpk_gt_u32 s17, 0x187f
	s_cbranch_scc0 .LBB0_39_hq
	s_cmpk_gt_u32 s17, 0x1a7f
	s_cbranch_scc0 .LBB0_40_hq
	s_cmpk_gt_u32 s17, 0x1e7f
	s_cbranch_scc0 .LBB0_41_hq
	s_lshl_b32 s1, s17, 6
	s_cmpk_gt_u32 s17, 0x5e7f
	s_cbranch_scc0 .LBB0_42_hq
	s_add_i32 s2, s17, 0xffffa180
	s_lshr_b32 s4, s2, 9
	s_lshl_b32 s2, s2, 1
	s_and_b32 s18, s2, 0x3c0
	s_load_dwordx2 s[2:3], s[8:9], 0x88
	s_lshl_b32 s5, s0, 4
	s_add_i32 s6, s4, s5
	s_mov_b32 s7, 0
	s_and_b32 s16, s1, 0x7c0
	s_lshl_b64 s[4:5], s[6:7], 23
	s_waitcnt lgkmcnt(0)
	s_add_u32 s4, s2, s4
	s_addc_u32 s5, s3, s5
	s_lshl_b64 s[2:3], s[6:7], 21
	s_add_u32 s2, s10, s2
	s_addc_u32 s3, s11, s3
	s_add_u32 s6, s2, 0x18600000
	v_lshl_or_b32 v0, v2, 2, s16
	s_addc_u32 s7, s3, 0
	s_mov_b64 s[2:3], 0
	s_branch .LBB0_43_hq

;     ...
;         auto decode = [&](int it) -> TrDesc {
;             TrDesc d; d.zero = 0; d.rope = 0; d.f8 = 0;
;             const int l = it / C_L; int r = it % C_L;
;             const float* W; unsigned char* WT; int ldw, K, k0, n0, scol, esz = 2;
;             if (r < C_IN) { const int kb = r / 188, nb = r % 188; n0 = 64 * nb; k0 = 64 * kb; ldw = NIN; K = D; W = a.w_in + (size_t)l * D * NIN;
;                 if (n0 < 3072) { d.rope = 1; scol = (n0 >> 7) * 128 + 32 * ((n0 >> 6) & 1) + 64 * (q4 >> 3) + 4 * (q4 & 7); }
;                 else if (n0 < 7680) scol = n0 + 4 * q4;
;                 else if (n0 < 11776) scol = n0 + 16 + 4 * q4;
;                 else if (n0 == 11776) { scol = (q4 < 4) ? 7680 + 4 * q4 : 0; d.zero = (q4 < 4) ? 0 : 1; }
;                 else { scol = 0; d.zero = 1; }
;     ...
;                 d.f8 = 1; esz = 1; WT = ws + WS_WIN + (size_t)l * NP * D;
;     ...
;                 WT = ws + WS_WIN + (size_t)l * NP * D * 2;
;     ...
;             } else if ((r -= C_IN) < C_OA) { const int kb = r / 32, nb = r % 32; n0 = 64 * nb; k0 = 64 * kb; ldw = D; K = 512; scol = n0 + 4 * q4; W = a.w_out_a + (size_t)l * 512 * D; WT = ws + WS_WOA + (size_t)l * D * 512 * (MIX_F8 ? 1 : 2); if (MIX_F8) { d.f8 = 1; esz = 1; }
;                 if (BR_FUSE) { K = 1536; WT = ws + WS_WOA + (size_t)l * D * 1536 + 1024; }
;             } else if ((r -= C_OA) < C_OB) { const int kb = r / 32, nb = r % 32; n0 = 64 * nb; k0 = 64 * kb; ldw = D; K = 1024; scol = n0 + 4 * q4; W = a.w_out_b + (size_t)l * 1024 * D; WT = ws + WS_WOB + (size_t)l * D * 1024 * (MIX_F8 ? 1 : 2); if (MIX_F8) { d.f8 = 1; esz = 1; }
;                 if (BR_FUSE) { K = 1536; WT = ws + WS_WOA + (size_t)l * D * 1536; }
;             } else if ((r -= C_OB) < C_O) { const int kb = r / 32, nb = r % 32; n0 = 64 * nb; k0 = 64 * kb; ldw = D; K = D; scol = n0 + 4 * q4; W = a.w_out + (size_t)l * D * D; WT = ws + WS_WO + (size_t)l * D * D * (MIX_F8 ? 1 : 2); if (MIX_F8) { d.f8 = 1; esz = 1; }
;     ...
;         while (it < NIT) {
;             const int itB = it + NGW;
;             if (itB < NIT) { dB = decode(NIT - 1 - itB); tr_load(dB, vB); }
;             tr_finish(dA, vA, scr, lane);
;             if (itB >= NIT) break;
;             const int itA = itB + NGW;
;             if (itA < NIT) { dA = decode(NIT - 1 - itA); tr_load(dA, vA); }
.LBB0_72_hq:
	s_cmp_ge_i32 s42, s101
	s_cbranch_scc1 .LBB0_70_hq
	s_lshr_b32 s44, s42, 6
	s_lshl_b32 s44, s44, 3
	s_bfe_u32 s100, s42, 0x30002
	s_or_b32 s44, s44, s100
	s_add_i32 s44, s44, 48
	s_and_b32 s100, s44, 7
	s_lshr_b32 s44, s44, 3
	s_lshl_b32 s44, s44, 6
	s_lshl_b32 s100, s100, 2
	s_or_b32 s44, s44, s100
	s_and_b32 s100, s42, 0x23
	s_or_b32 s44, s44, s100
	s_cmp_lt_i32 s44, s101
	s_cselect_b64 s[20:21], -1, 0
	s_cmp_ge_i32 s44, s101
	s_cselect_b64 s[12:13], -1, 0
	s_and_b64 vcc, exec, s[12:13]
	s_cbranch_vccnz .LBB0_106_hq
	s_sub_i32 s3, 0xfcff, s44
	s_mul_hi_u32 s0, s3, 0x81848da9
	s_lshr_b32 s0, s0, 14
	s_mul_i32 s14, s0, 0x7e80
	s_sub_i32 s45, s3, s14
	s_cmpk_gt_u32 s45, 0x177f
	s_cbranch_scc0 .LBB0_81_hq
	s_cmpk_gt_u32 s45, 0x187f
	s_cbranch_scc0 .LBB0_83_hq
	s_cmpk_gt_u32 s45, 0x1a7f
	s_cbranch_scc0 .LBB0_84_hq
	s_cmpk_gt_u32 s45, 0x1e7f
	s_cbranch_scc0 .LBB0_85_hq
	s_lshl_b32 s24, s45, 6
	s_cmpk_gt_u32 s45, 0x5e7f
	s_cbranch_scc0 .LBB0_121_hq
	s_add_i32 s14, s45, 0xffffa180
	s_lshr_b32 s18, s14, 9
	s_lshl_b32 s14, s14, 1
	s_and_b32 s49, s14, 0x3c0
	s_load_dwordx2 s[14:15], s[8:9], 0x88
	s_lshl_b32 s19, s0, 4
	s_add_i32 s22, s18, s19
	s_mov_b32 s23, s1
	s_and_b32 s3, s24, 0x7c0
	s_lshl_b64 s[18:19], s[22:23], 23
	s_waitcnt lgkmcnt(0)
	s_add_u32 s18, s14, s18
	s_addc_u32 s19, s15, s19
	s_lshl_b64 s[14:15], s[22:23], 21
	s_add_u32 s22, s28, s14
	v_or_b32_e32 v0, s3, v136
	s_addc_u32 s23, s29, s15
	s_cbranch_execz .LBB0_122_hq
	s_movk_i32 s14, 0x400
	s_mov_b64 s[24:25], 0x800
	s_cbranch_execz .LBB0_86_hq
	s_branch .LBB0_87_hq

; #define LAS __attribute__((address_space(3)))
; #define LDS_WAIT() asm volatile("s_waitcnt lgkmcnt(0)" ::: "memory")
; __device__ __forceinline__ unsigned pk_fp8x4(float a, float b, float c, float d) { int p = __builtin_amdgcn_cvt_pk_fp8_f32(sat8(a), sat8(b), 0, false); p = __builtin_amdgcn_cvt_pk_fp8_f32(sat8(c), sat8(d), p, true); return (unsigned)p; }
; __device__ __forceinline__ void tr_finish(const TrDesc& d, f32x4 (&v)[16], LAS float* scr, int lane) {
;     ...
;     const int d0 = d.rope ? 8 * (q4 & 7) + (q4 >> 3) : 4 * q4, ds = d.rope ? 2 : 1;
;     { LAS float* rp = scr + kk * 65 + d0;
; #pragma unroll
;         for (int i = 0; i < 16; ++i) { rp[4 * i * 65] = v[i][0]; rp[4 * i * 65 + ds] = v[i][1]; rp[4 * i * 65 + 2 * ds] = v[i][2]; rp[4 * i * 65 + 3 * ds] = v[i][3]; } }
;     LDS_WAIT(); asm volatile("" ::: "memory");
;     if (d.f8) {
;         const int c = lane & 3, nl = lane >> 2; const LAS float* sp = scr + (16 * c) * 65 + nl; unsigned char* dp = d.dst + (size_t)nl * d.K + 16 * c;
; #pragma unroll
;         for (int j = 0; j < 4; ++j) { u32x4 o;
;             o.x = pk_fp8x4(sp[0 * 65 + 16 * j] * 32.0f, sp[1 * 65 + 16 * j] * 32.0f, sp[2 * 65 + 16 * j] * 32.0f, sp[3 * 65 + 16 * j] * 32.0f);
;             o.y = pk_fp8x4(sp[4 * 65 + 16 * j] * 32.0f, sp[5 * 65 + 16 * j] * 32.0f, sp[6 * 65 + 16 * j] * 32.0f, sp[7 * 65 + 16 * j] * 32.0f);
;             o.z = pk_fp8x4(sp[8 * 65 + 16 * j] * 32.0f, sp[9 * 65 + 16 * j] * 32.0f, sp[10 * 65 + 16 * j] * 32.0f, sp[11 * 65 + 16 * j] * 32.0f);
;             o.w = pk_fp8x4(sp[12 * 65 + 16 * j] * 32.0f, sp[13 * 65 + 16 * j] * 32.0f, sp[14 * 65 + 16 * j] * 32.0f, sp[15 * 65 + 16 * j] * 32.0f);
.LBB0_108_hq:
	s_or_b64 exec, exec, s[22:23]
	s_cmp_eq_u32 s43, 0
	s_cselect_b64 vcc, -1, 0
	s_cmp_lg_u32 s43, 0
	s_cselect_b64 s[22:23], -1, 0
	v_cndmask_b32_e64 v2, 0, 1, s[22:23]
	s_and_b64 s[22:23], s[22:23], exec
	v_cndmask_b32_e32 v0, v140, v136, vcc
	s_cselect_b32 s0, 2, 1
	v_lshl_add_u32 v0, v0, 2, v141
	s_lshl_b32 s3, s0, 2
	v_add_u32_e32 v3, s3, v0
	v_lshlrev_b32_e64 v2, v2, 3
	s_waitcnt vmcnt(15)
	ds_write_b32 v3, v5
	v_lshl_add_u32 v3, s0, 3, v0
	v_lshl_add_u32 v2, v2, 2, v0
	v_subrev_u32_e32 v146, s3, v3
	ds_write_b32 v0, v4
	ds_write_b32 v3, v6
	ds_write_b32 v2, v7
	s_waitcnt vmcnt(14)
	ds_write_b32 v0, v8 offset:1040
	ds_write_b32 v146, v9 offset:1040
	ds_write_b32 v3, v10 offset:1040
	ds_write_b32 v2, v11 offset:1040
	s_waitcnt vmcnt(13)
	ds_write_b32 v0, v12 offset:2080
	ds_write_b32 v146, v13 offset:2080
	ds_write_b32 v3, v14 offset:2080
	ds_write_b32 v2, v15 offset:2080
	s_waitcnt vmcnt(12)
	ds_write_b32 v0, v16 offset:3120
	ds_write_b32 v146, v17 offset:3120
	ds_write_b32 v3, v18 offset:3120
	ds_write_b32 v2, v19 offset:3120
	s_waitcnt vmcnt(11)
	ds_write_b32 v0, v20 offset:4160
	ds_write_b32 v146, v21 offset:4160
	ds_write_b32 v3, v22 offset:4160
	ds_write_b32 v2, v23 offset:4160
	s_waitcnt vmcnt(10)
	ds_write_b32 v0, v24 offset:5200
	ds_write_b32 v146, v25 offset:5200
	ds_write_b32 v3, v26 offset:5200
	ds_write_b32 v2, v27 offset:5200
	s_waitcnt vmcnt(9)
	ds_write_b32 v0, v28 offset:6240
	ds_write_b32 v146, v29 offset:6240
	ds_write_b32 v3, v30 offset:6240
	ds_write_b32 v2, v31 offset:6240
	s_waitcnt vmcnt(8)
	ds_write_b32 v0, v32 offset:7280
	ds_write_b32 v146, v33 offset:7280
	ds_write_b32 v3, v34 offset:7280
	ds_write_b32 v2, v35 offset:7280
	s_waitcnt vmcnt(7)
	ds_write_b32 v0, v36 offset:8320
	ds_write_b32 v146, v37 offset:8320
	ds_write_b32 v3, v38 offset:8320
	ds_write_b32 v2, v39 offset:8320
	s_waitcnt vmcnt(6)
	ds_write_b32 v0, v40 offset:9360
	ds_write_b32 v146, v41 offset:9360
	ds_write_b32 v3, v42 offset:9360
	ds_write_b32 v2, v43 offset:9360
	s_waitcnt vmcnt(5)
	ds_write_b32 v0, v44 offset:10400
	ds_write_b32 v146, v45 offset:10400
	ds_write_b32 v3, v46 offset:10400
	ds_write_b32 v2, v47 offset:10400
	s_waitcnt vmcnt(4)
	ds_write_b32 v0, v48 offset:11440
	ds_write_b32 v146, v49 offset:11440
	ds_write_b32 v3, v50 offset:11440
	ds_write_b32 v2, v51 offset:11440
	s_waitcnt vmcnt(3)
	ds_write_b32 v0, v52 offset:12480
	ds_write_b32 v146, v53 offset:12480
	ds_write_b32 v3, v54 offset:12480
	ds_write_b32 v2, v55 offset:12480
	s_waitcnt vmcnt(2)
	ds_write_b32 v0, v56 offset:13520
	ds_write_b32 v146, v57 offset:13520
	ds_write_b32 v3, v58 offset:13520
	ds_write_b32 v2, v59 offset:13520
	s_waitcnt vmcnt(1)
	ds_write_b32 v0, v60 offset:14560
	ds_write_b32 v146, v61 offset:14560
	ds_write_b32 v3, v62 offset:14560
	ds_write_b32 v2, v63 offset:14560
	s_waitcnt vmcnt(0)
	ds_write_b32 v0, v64 offset:15600
	ds_write_b32 v146, v65 offset:15600
	ds_write_b32 v3, v66 offset:15600
	ds_write_b32 v2, v67 offset:15600
	s_waitcnt lgkmcnt(0)
	ds_read2_b32 v[2:3], v142 offset1:16
	ds_read2_b32 v[148:149], v142 offset0:65 offset1:81
	ds_read2_b32 v[154:155], v142 offset0:130 offset1:146
	ds_read2_b32 v[156:157], v142 offset0:195 offset1:211
	v_mov_b32_e32 v150, 0
	s_waitcnt lgkmcnt(3)
	v_mul_f32_e32 v0, 0x42000000, v2
	s_waitcnt lgkmcnt(2)
	v_mul_f32_e32 v2, 0x42000000, v148
	v_med3_f32 v0, v0, s41, v143
	s_waitcnt lgkmcnt(0)
	v_mul_f32_e32 v147, 0x42000000, v156
	v_med3_f32 v2, v2, s41, v143
	v_cvt_pk_fp8_f32 v150, v0, v2
	v_med3_f32 v2, v147, s41, v143
	v_add_u32_e32 v147, 0x400, v142
	ds_read2_b32 v[160:161], v147 offset0:4 offset1:20
	ds_read2_b32 v[162:163], v147 offset0:69 offset1:85
	ds_read2_b32 v[164:165], v147 offset0:134 offset1:150
	ds_read2_b32 v[166:167], v147 offset0:199 offset1:215
	v_mul_f32_e32 v146, 0x42000000, v154
	v_med3_f32 v0, v146, s41, v143
	v_cvt_pk_fp8_f32 v150, v0, v2 op_sel:[0,0,1]
	s_waitcnt lgkmcnt(3)
	v_mul_f32_e32 v0, 0x42000000, v160
	s_waitcnt lgkmcnt(2)
	v_mul_f32_e32 v2, 0x42000000, v162
	s_waitcnt lgkmcnt(0)
	v_mul_f32_e32 v148, 0x42000000, v166
	v_med3_f32 v0, v0, s41, v143
	v_med3_f32 v2, v2, s41, v143
	v_mov_b32_e32 v151, 0
	v_cvt_pk_fp8_f32 v151, v0, v2
	v_med3_f32 v2, v148, s41, v143
	v_add_u32_e32 v148, 0x800, v142
	ds_read2_b32 v[168:169], v148 offset0:8 offset1:24
	ds_read2_b32 v[170:171], v148 offset0:73 offset1:89
	ds_read2_b32 v[172:173], v148 offset0:138 offset1:154
	ds_read2_b32 v[174:175], v148 offset0:203 offset1:219
	v_mul_f32_e32 v146, 0x42000000, v164
	v_med3_f32 v0, v146, s41, v143
	v_cvt_pk_fp8_f32 v151, v0, v2 op_sel:[0,0,1]
	s_waitcnt lgkmcnt(3)
	v_mul_f32_e32 v0, 0x42000000, v168
	s_waitcnt lgkmcnt(2)
	v_mul_f32_e32 v2, 0x42000000, v170
	s_waitcnt lgkmcnt(1)
	v_mul_f32_e32 v146, 0x42000000, v172
	v_med3_f32 v0, v0, s41, v143
	v_med3_f32 v2, v2, s41, v143
	v_mov_b32_e32 v152, 0
	v_cvt_pk_fp8_f32 v152, v0, v2
	v_med3_f32 v0, v146, s41, v143
	v_add_u32_e32 v146, 0xc00, v142
	ds_read2_b32 v[176:177], v146 offset0:12 offset1:28
	ds_read2_b32 v[178:179], v146 offset0:77 offset1:93
	ds_read2_b32 v[180:181], v146 offset0:142 offset1:158
	s_waitcnt lgkmcnt(3)
	v_mul_f32_e32 v153, 0x42000000, v174
	v_med3_f32 v2, v153, s41, v143
	ds_read2_b32 v[182:183], v146 offset0:207 offset1:223
	v_cvt_pk_fp8_f32 v152, v0, v2 op_sel:[0,0,1]
	s_waitcnt lgkmcnt(3)
	v_mul_f32_e32 v0, 0x42000000, v176
	s_waitcnt lgkmcnt(2)
	v_mul_f32_e32 v2, 0x42000000, v178
	v_med3_f32 v0, v0, s41, v143
	v_med3_f32 v2, v2, s41, v143
	v_mov_b32_e32 v153, 0
	v_cvt_pk_fp8_f32 v153, v0, v2
	s_waitcnt lgkmcnt(1)
	v_mul_f32_e32 v154, 0x42000000, v180
	s_waitcnt lgkmcnt(0)
; #define LAS __attribute__((address_space(3)))
; #define GAS __attribute__((address_space(1)))
; __device__ __forceinline__ unsigned pk_fp8x4(float a, float b, float c, float d) { int p = __builtin_amdgcn_cvt_pk_fp8_f32(sat8(a), sat8(b), 0, false); p = __builtin_amdgcn_cvt_pk_fp8_f32(sat8(c), sat8(d), p, true); return (unsigned)p; }
; __device__ __forceinline__ void tr_finish(const TrDesc& d, f32x4 (&v)[16], LAS float* scr, int lane) {
;     ...
;         const int c = lane & 3, nl = lane >> 2; const LAS float* sp = scr + (16 * c) * 65 + nl; unsigned char* dp = d.dst + (size_t)nl * d.K + 16 * c;
; #pragma unroll
;         for (int j = 0; j < 4; ++j) { u32x4 o;
;             o.x = pk_fp8x4(sp[0 * 65 + 16 * j] * 32.0f, sp[1 * 65 + 16 * j] * 32.0f, sp[2 * 65 + 16 * j] * 32.0f, sp[3 * 65 + 16 * j] * 32.0f);
;             o.y = pk_fp8x4(sp[4 * 65 + 16 * j] * 32.0f, sp[5 * 65 + 16 * j] * 32.0f, sp[6 * 65 + 16 * j] * 32.0f, sp[7 * 65 + 16 * j] * 32.0f);
;             o.z = pk_fp8x4(sp[8 * 65 + 16 * j] * 32.0f, sp[9 * 65 + 16 * j] * 32.0f, sp[10 * 65 + 16 * j] * 32.0f, sp[11 * 65 + 16 * j] * 32.0f);
;             o.w = pk_fp8x4(sp[12 * 65 + 16 * j] * 32.0f, sp[13 * 65 + 16 * j] * 32.0f, sp[14 * 65 + 16 * j] * 32.0f, sp[15 * 65 + 16 * j] * 32.0f);
;             *(GAS u32x4*)(dp + (size_t)(16 * j) * d.K) = o; }
	v_mul_f32_e32 v0, 0x42000000, v182
	v_med3_f32 v2, v154, s41, v143
	v_med3_f32 v0, v0, s41, v143
	v_cvt_pk_fp8_f32 v153, v2, v0 op_sel:[0,0,1]
	v_mov_b64_e32 v[158:159], s[16:17]
	v_mad_i64_i32 v[158:159], s[22:23], s2, v132, v[158:159]
	v_lshl_add_u64 v[158:159], v[158:159], 0, v[134:135]
	v_mul_f32_e32 v0, 0x42000000, v3
	v_mul_f32_e32 v2, 0x42000000, v149
	global_store_dwordx4 v[158:159], v[150:153], off nt
	v_med3_f32 v0, v0, s41, v143
	v_med3_f32 v2, v2, s41, v143
	v_mov_b32_e32 v150, 0
	v_cvt_pk_fp8_f32 v150, v0, v2
	v_mul_f32_e32 v3, 0x42000000, v155
	v_mul_f32_e32 v0, 0x42000000, v157
	v_med3_f32 v2, v3, s41, v143
	v_med3_f32 v0, v0, s41, v143
	v_cvt_pk_fp8_f32 v150, v2, v0 op_sel:[0,0,1]
	v_mul_f32_e32 v0, 0x42000000, v161
	v_mul_f32_e32 v2, 0x42000000, v163
	v_med3_f32 v0, v0, s41, v143
	v_med3_f32 v2, v2, s41, v143
	v_mov_b32_e32 v151, 0
	v_cvt_pk_fp8_f32 v151, v0, v2
	v_mul_f32_e32 v3, 0x42000000, v165
	v_mul_f32_e32 v0, 0x42000000, v167
	v_med3_f32 v2, v3, s41, v143
	v_med3_f32 v0, v0, s41, v143
	v_cvt_pk_fp8_f32 v151, v2, v0 op_sel:[0,0,1]
	v_mul_f32_e32 v0, 0x42000000, v169
	v_mul_f32_e32 v2, 0x42000000, v171
	v_med3_f32 v0, v0, s41, v143
	v_med3_f32 v2, v2, s41, v143
	v_mov_b32_e32 v152, 0
	v_cvt_pk_fp8_f32 v152, v0, v2
	v_mul_f32_e32 v3, 0x42000000, v173
	v_mul_f32_e32 v0, 0x42000000, v175
	v_med3_f32 v2, v3, s41, v143
	v_med3_f32 v0, v0, s41, v143
	v_cvt_pk_fp8_f32 v152, v2, v0 op_sel:[0,0,1]
	v_mul_f32_e32 v0, 0x42000000, v177
	v_mul_f32_e32 v2, 0x42000000, v179
	v_med3_f32 v0, v0, s41, v143
	v_med3_f32 v2, v2, s41, v143
	v_mov_b32_e32 v153, 0
	v_cvt_pk_fp8_f32 v153, v0, v2
	s_ashr_i32 s3, s2, 31
	v_mul_f32_e32 v3, 0x42000000, v181
	v_mul_f32_e32 v0, 0x42000000, v183
	v_med3_f32 v2, v3, s41, v143
	v_med3_f32 v0, v0, s41, v143
	s_lshl_b64 s[22:23], s[2:3], 4
	v_cvt_pk_fp8_f32 v153, v2, v0 op_sel:[0,0,1]
	v_lshl_add_u64 v[2:3], v[158:159], 0, s[22:23]
	ds_read2_b32 v[154:155], v142 offset0:32 offset1:48
	ds_read2_b32 v[156:157], v142 offset0:97 offset1:113
	ds_read2_b32 v[158:159], v142 offset0:162 offset1:178
	ds_read2_b32 v[160:161], v142 offset0:227 offset1:243
	s_andn2_b64 vcc, exec, s[20:21]
	s_waitcnt lgkmcnt(3)
	v_mul_f32_e32 v0, 0x42000000, v154
	s_waitcnt lgkmcnt(2)
	v_mul_f32_e32 v149, 0x42000000, v156
	global_store_dwordx4 v[2:3], v[150:153], off nt
	v_med3_f32 v0, v0, s41, v143
	v_med3_f32 v149, v149, s41, v143
	v_mov_b32_e32 v150, 0
	v_cvt_pk_fp8_f32 v150, v0, v149
	ds_read2_b32 v[162:163], v147 offset0:36 offset1:52
	ds_read2_b32 v[164:165], v147 offset0:101 offset1:117
	ds_read2_b32 v[166:167], v147 offset0:166 offset1:182
	ds_read2_b32 v[168:169], v147 offset0:231 offset1:247
	s_waitcnt lgkmcnt(5)
	v_mul_f32_e32 v151, 0x42000000, v158
	s_waitcnt lgkmcnt(4)
	v_mul_f32_e32 v152, 0x42000000, v160
	v_med3_f32 v0, v151, s41, v143
	v_med3_f32 v149, v152, s41, v143
	v_cvt_pk_fp8_f32 v150, v0, v149 op_sel:[0,0,1]
	s_waitcnt lgkmcnt(3)
	v_mul_f32_e32 v0, 0x42000000, v162
	s_waitcnt lgkmcnt(2)
	v_mul_f32_e32 v149, 0x42000000, v164
	v_med3_f32 v0, v0, s41, v143
	v_med3_f32 v149, v149, s41, v143
	v_mov_b32_e32 v151, 0
	v_cvt_pk_fp8_f32 v151, v0, v149
	ds_read2_b32 v[170:171], v148 offset0:40 offset1:56
	ds_read2_b32 v[172:173], v148 offset0:105 offset1:121
	ds_read2_b32 v[174:175], v148 offset0:170 offset1:186
	ds_read2_b32 v[176:177], v148 offset0:235 offset1:251
	s_waitcnt lgkmcnt(5)
	v_mul_f32_e32 v152, 0x42000000, v166
	s_waitcnt lgkmcnt(4)
	v_mul_f32_e32 v153, 0x42000000, v168
	v_med3_f32 v0, v152, s41, v143
	v_med3_f32 v149, v153, s41, v143
	v_cvt_pk_fp8_f32 v151, v0, v149 op_sel:[0,0,1]
	s_waitcnt lgkmcnt(3)
	v_mul_f32_e32 v0, 0x42000000, v170
	s_waitcnt lgkmcnt(2)
	v_mul_f32_e32 v149, 0x42000000, v172
	v_med3_f32 v0, v0, s41, v143
	v_med3_f32 v149, v149, s41, v143
	v_mov_b32_e32 v152, 0
	v_cvt_pk_fp8_f32 v152, v0, v149
	ds_read2_b32 v[178:179], v146 offset0:44 offset1:60
	ds_read2_b32 v[180:181], v146 offset0:109 offset1:125
	ds_read2_b32 v[182:183], v146 offset0:174 offset1:190
	s_waitcnt lgkmcnt(4)
	v_mul_f32_e32 v153, 0x42000000, v174
	s_waitcnt lgkmcnt(3)
	v_mul_f32_e32 v154, 0x42000000, v176
	v_med3_f32 v0, v153, s41, v143
	v_med3_f32 v149, v154, s41, v143
	ds_read2_b32 v[184:185], v146 offset0:239 offset1:255
	v_cvt_pk_fp8_f32 v152, v0, v149 op_sel:[0,0,1]
	s_waitcnt lgkmcnt(3)
	v_mul_f32_e32 v0, 0x42000000, v178
	s_waitcnt lgkmcnt(2)
	v_mul_f32_e32 v149, 0x42000000, v180
	v_med3_f32 v0, v0, s41, v143
	v_med3_f32 v149, v149, s41, v143
	v_mov_b32_e32 v153, 0
	v_cvt_pk_fp8_f32 v153, v0, v149
	s_waitcnt lgkmcnt(1)
	v_mul_f32_e32 v154, 0x42000000, v182
	s_waitcnt lgkmcnt(0)
	v_mul_f32_e32 v0, 0x42000000, v184
	v_med3_f32 v149, v154, s41, v143
	v_med3_f32 v0, v0, s41, v143
	v_cvt_pk_fp8_f32 v153, v149, v0 op_sel:[0,0,1]
	v_mul_f32_e32 v0, 0x42000000, v155
	v_mul_f32_e32 v149, 0x42000000, v157
	v_med3_f32 v0, v0, s41, v143
	v_med3_f32 v149, v149, s41, v143
	v_mov_b32_e32 v154, 0
	v_cvt_pk_fp8_f32 v154, v0, v149
	v_mul_f32_e32 v155, 0x42000000, v159
	v_mul_f32_e32 v0, 0x42000000, v161
	v_med3_f32 v149, v155, s41, v143
	v_med3_f32 v0, v0, s41, v143
	v_cvt_pk_fp8_f32 v154, v149, v0 op_sel:[0,0,1]
	v_mul_f32_e32 v0, 0x42000000, v163
	v_mul_f32_e32 v149, 0x42000000, v165
	v_med3_f32 v0, v0, s41, v143
	v_med3_f32 v149, v149, s41, v143
	v_mov_b32_e32 v155, 0
	v_cvt_pk_fp8_f32 v155, v0, v149
	v_mul_f32_e32 v156, 0x42000000, v167
	v_mul_f32_e32 v0, 0x42000000, v169
	v_med3_f32 v149, v156, s41, v143
	v_med3_f32 v0, v0, s41, v143
	v_cvt_pk_fp8_f32 v155, v149, v0 op_sel:[0,0,1]
	v_mul_f32_e32 v0, 0x42000000, v171
	v_mul_f32_e32 v149, 0x42000000, v173
	v_med3_f32 v0, v0, s41, v143
	v_med3_f32 v149, v149, s41, v143
	v_mov_b32_e32 v156, 0
	v_cvt_pk_fp8_f32 v156, v0, v149
	v_mul_f32_e32 v157, 0x42000000, v175
	v_mul_f32_e32 v0, 0x42000000, v177
	v_med3_f32 v149, v157, s41, v143
	v_med3_f32 v0, v0, s41, v143
	v_cvt_pk_fp8_f32 v156, v149, v0 op_sel:[0,0,1]
	v_mul_f32_e32 v0, 0x42000000, v179
	v_mul_f32_e32 v149, 0x42000000, v181
	v_med3_f32 v0, v0, s41, v143
	v_med3_f32 v149, v149, s41, v143
	v_mov_b32_e32 v157, 0
	v_cvt_pk_fp8_f32 v157, v0, v149
	v_mul_f32_e32 v158, 0x42000000, v183
	v_mul_f32_e32 v0, 0x42000000, v185
	v_med3_f32 v149, v158, s41, v143
	v_med3_f32 v0, v0, s41, v143
	v_cvt_pk_fp8_f32 v157, v149, v0 op_sel:[0,0,1]
	v_lshl_add_u64 v[2:3], v[2:3], 0, s[22:23]
	global_store_dwordx4 v[2:3], v[150:153], off nt
	v_lshl_add_u64 v[2:3], v[2:3], 0, s[22:23]
	global_store_dwordx4 v[2:3], v[154:157], off nt
	s_waitcnt lgkmcnt(0)
	s_cbranch_vccnz .LBB0_71_hq
;     ...
;         auto decode = [&](int it) -> TrDesc {
;             TrDesc d; d.zero = 0; d.rope = 0; d.f8 = 0;
;             const int l = it / C_L; int r = it % C_L;
;             const float* W; unsigned char* WT; int ldw, K, k0, n0, scol, esz = 2;
;             if (r < C_IN) { const int kb = r / 188, nb = r % 188; n0 = 64 * nb; k0 = 64 * kb; ldw = NIN; K = D; W = a.w_in + (size_t)l * D * NIN;
;                 if (n0 < 3072) { d.rope = 1; scol = (n0 >> 7) * 128 + 32 * ((n0 >> 6) & 1) + 64 * (q4 >> 3) + 4 * (q4 & 7); }
;                 else if (n0 < 7680) scol = n0 + 4 * q4;
;                 else if (n0 < 11776) scol = n0 + 16 + 4 * q4;
;                 else if (n0 == 11776) { scol = (q4 < 4) ? 7680 + 4 * q4 : 0; d.zero = (q4 < 4) ? 0 : 1; }
;                 else { scol = 0; d.zero = 1; }
;     ...
;                 d.f8 = 1; esz = 1; WT = ws + WS_WIN + (size_t)l * NP * D;
;     ...
;                 WT = ws + WS_WIN + (size_t)l * NP * D * 2;
;     ...
;             } else if ((r -= C_IN) < C_OA) { const int kb = r / 32, nb = r % 32; n0 = 64 * nb; k0 = 64 * kb; ldw = D; K = 512; scol = n0 + 4 * q4; W = a.w_out_a + (size_t)l * 512 * D; WT = ws + WS_WOA + (size_t)l * D * 512 * (MIX_F8 ? 1 : 2); if (MIX_F8) { d.f8 = 1; esz = 1; }
;                 if (BR_FUSE) { K = 1536; WT = ws + WS_WOA + (size_t)l * D * 1536 + 1024; }
;             } else if ((r -= C_OA) < C_OB) { const int kb = r / 32, nb = r % 32; n0 = 64 * nb; k0 = 64 * kb; ldw = D; K = 1024; scol = n0 + 4 * q4; W = a.w_out_b + (size_t)l * 1024 * D; WT = ws + WS_WOB + (size_t)l * D * 1024 * (MIX_F8 ? 1 : 2); if (MIX_F8) { d.f8 = 1; esz = 1; }
;                 if (BR_FUSE) { K = 1536; WT = ws + WS_WOA + (size_t)l * D * 1536; }
;             } else if ((r -= C_OB) < C_O) { const int kb = r / 32, nb = r % 32; n0 = 64 * nb; k0 = 64 * kb; ldw = D; K = D; scol = n0 + 4 * q4; W = a.w_out + (size_t)l * D * D; WT = ws + WS_WO + (size_t)l * D * D * (MIX_F8 ? 1 : 2); if (MIX_F8) { d.f8 = 1; esz = 1; }
;             } else if ((r -= C_O) < C_GU) { const int e = r / 1024, r2 = r % 1024, kb = r2 / 32, nb = r2 % 32, pn = nb >> 2, sgu = (nb >> 1) & 1, c0 = 64 * (nb & 1);
;     ...
;             if (itB >= NIT) break;
;             const int itA = itB + NGW;
;             if (itA < NIT) { dA = decode(NIT - 1 - itA); tr_load(dA, vA); }
;             tr_finish(dB, vB, scr, lane);
;             it = itA;
;         }
	s_lshr_b32 s42, s44, 6
	s_lshl_b32 s42, s42, 3
	s_bfe_u32 s100, s44, 0x30002
	s_or_b32 s42, s42, s100
	s_add_i32 s42, s42, 48
	s_and_b32 s100, s42, 7
	s_lshr_b32 s42, s42, 3
	s_lshl_b32 s42, s42, 6
	s_lshl_b32 s100, s100, 2
	s_or_b32 s42, s42, s100
	s_and_b32 s100, s44, 0x23
	s_or_b32 s42, s42, s100
	s_cmp_ge_i32 s42, s101
	s_cbranch_scc1 .LBB0_144_hq
	s_sub_i32 s2, 0xfcff, s42
	s_mul_hi_u32 s0, s2, 0x81848da9
	s_lshr_b32 s0, s0, 14
	s_mul_i32 s3, s0, 0x7e80
	s_sub_i32 s27, s2, s3
	s_cmpk_gt_u32 s27, 0x177f
	s_cbranch_scc0 .LBB0_117_hq
	s_cmpk_gt_u32 s27, 0x187f
	s_cbranch_scc0 .LBB0_119_hq
	s_cmpk_gt_u32 s27, 0x1a7f
	s_cbranch_scc0 .LBB0_120_hq
	s_cmpk_gt_u32 s27, 0x1e7f
	s_cbranch_scc0 .LBB0_123_hq
	s_lshl_b32 s22, s27, 6
	s_cmpk_gt_u32 s27, 0x5e7f
	s_cbranch_scc0 .LBB0_147_hq
	s_add_i32 s2, s27, 0xffffa180
	s_lshr_b32 s16, s2, 9
	s_lshl_b32 s2, s2, 1
	s_and_b32 s44, s2, 0x3c0
	s_load_dwordx2 s[2:3], s[8:9], 0x88
	s_lshl_b32 s17, s0, 4
	s_add_i32 s20, s16, s17
	s_mov_b32 s21, s1
	s_and_b32 s15, s22, 0x7c0
	s_lshl_b64 s[16:17], s[20:21], 23
	s_waitcnt lgkmcnt(0)
	s_add_u32 s16, s2, s16
	s_addc_u32 s17, s3, s17
	s_lshl_b64 s[2:3], s[20:21], 21
	s_add_u32 s20, s28, s2
	v_or_b32_e32 v0, s15, v136
	s_addc_u32 s21, s29, s3
	s_cbranch_execz .LBB0_148_hq
	s_movk_i32 s2, 0x400
	s_mov_b64 s[22:23], 0x800
	s_cbranch_execz .LBB0_124_hq
	s_branch .LBB0_125_hq

; #define LAS __attribute__((address_space(3)))
; #define FRESH_TID() do { ap = fresh_args(); ws = ap->ws; unsigned m1_ = ~0u; asm volatile("" : "+s"(m1_)); lane = (int)__builtin_amdgcn_mbcnt_hi(m1_, __builtin_amdgcn_mbcnt_lo(m1_, 0u)); asm volatile("" : "+v"(lane)); wave = wave0; tid = wave0 * 64 + lane; } while (0)
; __device__ __forceinline__ void moe_table_build(LAS unsigned char* lds, const unsigned* cnt, int tid) {
;     ...
;     if (tid == 0) { int acc = 0; for (int e = 0; e < NE; ++e) { acc += (((LAS int*)(lds + MOE_TAB_OFF))[16 + e] + 255) >> 8; ((LAS int*)(lds + MOE_TAB_OFF))[e] = acc; } }
;     __syncthreads();
; }
;     __device__ __forceinline__ void init(LAS unsigned char* lds_, int nN_, int G_, int c_) {
;         lds = lds_; NT = __builtin_amdgcn_readfirstlane(((LAS int*)(lds + MOE_TAB_OFF))[15]); nN = nN_; G = G_; c = c_; }
; template <unsigned MASK, bool ONE>
; __global__ void __launch_bounds__(NTHREADS, 2) fwd_kernel(Args a_unused) {
;     ...
;         if (IN(P + 8, 9)) { FRESH_TID();
;             pg8::moe_table_build(lds, cntl, tid);
;             pg8::MoeOrder S; S.init(lds, 8, G, bx); pg8::RowsGather AM{rlist, lds}; pg8::EpiSwiGLU8 E{(unsigned char*)act};
;             pg8::gemm_phase<pg8::EpiSwiGLU8, pg8::MoeOrder, pg8::RowsGather, true, true>(lds, tid, hbuf, (const bf16_t*)(ws + WS_WGU + (size_t)l * NE * 2048 * D), (size_t)2048 * D / 2, D / 2, S, AM, E);
.LBB0_929:
	s_or_b64 exec, exec, s[0:1]
	v_readlane_b32 s0, v254, 58
	s_waitcnt lgkmcnt(0)
	s_barrier
	v_mov_b32_e32 v2, s0
	ds_read_b32 v2, v2
	v_readlane_b32 s1, v253, 4
	v_readfirstlane_b32 s14, v1
	s_waitcnt lgkmcnt(0)
	v_readfirstlane_b32 s22, v2
	s_lshl_b32 s0, s22, 3
	s_cmp_eq_u32 s101, 0
	s_cbranch_scc1 .Lno_help9
	s_cmpk_lt_i32 s1, 0xa0
	s_cbranch_scc1 .Lno_help9
	s_mov_b32 s100, 0x2a00
	s_mov_b32 s101, 0x8a80
	s_mov_b32 s0, 0
	v_writelane_b32 v251, s0, 30
	s_movk_i32 s0, 96
	s_branch .Lhp_entry

; #define LAS __attribute__((address_space(3)))
; #define FRESH_TID() do { ap = fresh_args(); ws = ap->ws; unsigned m1_ = ~0u; asm volatile("" : "+s"(m1_)); lane = (int)__builtin_amdgcn_mbcnt_hi(m1_, __builtin_amdgcn_mbcnt_lo(m1_, 0u)); asm volatile("" : "+v"(lane)); wave = wave0; tid = wave0 * 64 + lane; } while (0)
; __device__ __forceinline__ void moe_table_build(LAS unsigned char* lds, const unsigned* cnt, int tid) {
;     ...
;     if (tid == 0) { int acc = 0; for (int e = 0; e < NE; ++e) { acc += (((LAS int*)(lds + MOE_TAB_OFF))[16 + e] + 255) >> 8; ((LAS int*)(lds + MOE_TAB_OFF))[e] = acc; } }
;     __syncthreads();
; }
;     __device__ __forceinline__ void init(LAS unsigned char* lds_, int nN_, int G_, int c_) {
;         lds = lds_; NT = __builtin_amdgcn_readfirstlane(((LAS int*)(lds + MOE_TAB_OFF))[15]); nN = nN_; G = G_; c = c_; }
; template <unsigned MASK, bool ONE>
; __global__ void __launch_bounds__(NTHREADS, 2) fwd_kernel(Args a_unused) {
;     ...
;         if (IN(P + 9, 10)) { FRESH_TID();
;             pg8::moe_table_build(lds, cntl, tid);
;             pg8::MoeOrder S; S.init(lds, 8, G, bx); pg8::RowsContig AM; pg8::EpiPlainS E{Y, pg8::W8_INV};
;             pg8::gemm_phase<pg8::EpiPlainS, pg8::MoeOrder, pg8::RowsContig, true, true>(lds, tid, act, (const bf16_t*)(ws + WS_WDN + (size_t)l * NE * D * FF), (size_t)D * FF / 2, FF / 2, S, AM, E);
.LBB0_1010:
	s_or_b64 exec, exec, s[0:1]
	v_readlane_b32 s0, v254, 58
	s_waitcnt lgkmcnt(0)
	s_barrier
	v_mov_b32_e32 v2, s0
	ds_read_b32 v2, v2
	v_readlane_b32 s1, v253, 4
	v_readfirstlane_b32 s14, v1
	v_readlane_b32 s65, v255, 22
	s_movk_i32 s66, 0x179
	s_waitcnt lgkmcnt(0)
	v_readfirstlane_b32 s16, v2
	s_lshl_b32 s0, s16, 3
	s_cmp_eq_u32 s101, 0
	s_cbranch_scc1 .Lno_help10
	s_cmpk_lt_i32 s1, 0xc0
	s_cbranch_scc1 .Lno_help10
	s_mov_b32 s100, 0x800
	s_mov_b32 s101, 0x2a00
	s_mov_b32 s62, 0x20600000
	s_mov_b32 s0, 1
	v_writelane_b32 v251, s0, 30
	s_movk_i32 s0, 64
	s_branch .Lhp_entry
